# v18 plus P1/P8 unit-loop headers: compiler's vmcnt(2/1/0) ladder before the first fragment reads removed (it only guards kernel-entry arg loads, but drained the epilogue stores every unit)
# baseline (speedup 1.0000x reference)
.LBB0_260:
	s_ashr_i32 s41, s40, 31
	s_lshl_b64 s[42:43], s[40:41], 19
	s_add_u32 s42, s54, s42
	s_addc_u32 s43, s55, s43
	s_and_b64 s[44:45], s[4:5], exec
	ds_read_b128 v[0:3], v219
	ds_read_b128 v[4:7], v219 offset:1024
	ds_read_b128 v[8:11], v219 offset:2048
	ds_read_b128 v[12:15], v219 offset:3072
	ds_read_b128 v[16:19], v220
	ds_read_b128 v[20:23], v220 offset:1024
	ds_read_b128 v[24:27], v220 offset:2048
	ds_read_b128 v[28:31], v220 offset:3072
	s_cselect_b32 s7, s43, s13
	s_cselect_b32 s11, s42, s12
	s_ashr_i32 s39, s38, 31
	s_lshl_b64 s[44:45], s[38:39], 19
	s_add_u32 s44, s56, s44
	s_addc_u32 s45, s57, s45
	s_and_b64 s[46:47], s[4:5], exec
	s_cselect_b32 s39, s45, s9
	s_cselect_b32 s41, s44, s8
	s_add_u32 s46, s12, 0x100
	s_addc_u32 s47, s13, 0
	s_add_u32 s52, s8, 0x100
	s_addc_u32 s53, s9, 0
	s_add_u32 s48, s12, 0x180
	s_addc_u32 s49, s13, 0
	ds_read_b128 v[32:35], v221
	ds_read_b128 v[36:39], v221 offset:1024
	ds_read_b128 v[40:43], v221 offset:2048
	ds_read_b128 v[44:47], v221 offset:3072
	ds_read_b128 v[48:51], v221 offset:4096
	ds_read_b128 v[52:55], v221 offset:5120
	ds_read_b128 v[56:59], v221 offset:6144
	ds_read_b128 v[60:63], v221 offset:7168
	s_add_u32 s50, s8, 0x180
	s_addc_u32 s51, s9, 0
	s_add_u32 s76, s12, 0x40080
	s_addc_u32 s77, s13, 0
	s_add_i32 m0, s59, 0xc000
	s_nop 0
	global_load_lds_dwordx4 v215, s[76:77]
	s_nop 0
	s_add_i32 m0, s59, 0xe000
	s_nop 0
	global_load_lds_dwordx4 v217, s[76:77]
	s_waitcnt vmcnt(8) lgkmcnt(0)
	s_barrier
	s_waitcnt lgkmcnt(7)
	v_mfma_i32_16x16x64_i8 v[64:67], v[0:3], v[32:35], 0
	s_mov_b32 s76, 0
	v_mfma_i32_16x16x64_i8 v[68:71], v[8:11], v[32:35], 0
	s_waitcnt lgkmcnt(5)
	v_mfma_i32_16x16x64_i8 v[72:75], v[0:3], v[40:43], 0
	v_mfma_i32_16x16x64_i8 v[76:79], v[8:11], v[40:43], 0
	s_waitcnt lgkmcnt(3)
	v_mfma_i32_16x16x64_i8 v[84:87], v[8:11], v[48:51], 0
	s_waitcnt lgkmcnt(1)
	v_mfma_i32_16x16x64_i8 v[88:91], v[0:3], v[56:59], 0
	v_mfma_i32_16x16x64_i8 v[140:143], v[4:7], v[36:39], v[64:67]
	v_mfma_i32_16x16x64_i8 v[144:147], v[12:15], v[36:39], v[68:71]
	v_mfma_i32_16x16x64_i8 v[152:155], v[4:7], v[44:47], v[72:75]
	v_mfma_i32_16x16x64_i8 v[156:159], v[12:15], v[44:47], v[76:79]
	v_mfma_i32_16x16x64_i8 v[80:83], v[0:3], v[48:51], 0
	v_mfma_i32_16x16x64_i8 v[84:87], v[12:15], v[52:55], v[84:87]
	s_waitcnt lgkmcnt(0)
	v_mfma_i32_16x16x64_i8 v[88:91], v[4:7], v[60:63], v[88:91]
	v_mfma_i32_16x16x64_i8 v[92:95], v[8:11], v[56:59], 0
	v_mfma_i32_16x16x64_i8 v[80:83], v[4:7], v[52:55], v[80:83]
	v_mfma_i32_16x16x64_i8 v[92:95], v[12:15], v[60:63], v[92:95]
	v_mfma_i32_16x16x64_i8 v[96:99], v[16:19], v[32:35], 0
	v_mfma_i32_16x16x64_i8 v[32:35], v[24:27], v[32:35], 0
	v_mfma_i32_16x16x64_i8 v[96:99], v[20:23], v[36:39], v[96:99]
	v_mfma_i32_16x16x64_i8 v[32:35], v[28:31], v[36:39], v[32:35]
	v_mfma_i32_16x16x64_i8 v[36:39], v[16:19], v[40:43], 0
	v_mfma_i32_16x16x64_i8 v[40:43], v[24:27], v[40:43], 0
	v_mfma_i32_16x16x64_i8 v[36:39], v[20:23], v[44:47], v[36:39]
	v_mfma_i32_16x16x64_i8 v[40:43], v[28:31], v[44:47], v[40:43]
	v_mfma_i32_16x16x64_i8 v[44:47], v[16:19], v[48:51], 0
	v_mfma_i32_16x16x64_i8 v[48:51], v[24:27], v[48:51], 0
	v_mfma_i32_16x16x64_i8 v[44:47], v[20:23], v[52:55], v[44:47]
	v_mfma_i32_16x16x64_i8 v[48:51], v[28:31], v[52:55], v[48:51]
	v_mfma_i32_16x16x64_i8 v[52:55], v[16:19], v[56:59], 0
	v_mfma_i32_16x16x64_i8 v[56:59], v[24:27], v[56:59], 0
	v_mfma_i32_16x16x64_i8 v[52:55], v[20:23], v[60:63], v[52:55]
	v_mfma_i32_16x16x64_i8 v[56:59], v[28:31], v[60:63], v[56:59]
	s_barrier
	ds_read_b128 v[60:63], v221 offset:16384
	ds_read_b128 v[100:103], v221 offset:17408
	ds_read_b128 v[104:107], v221 offset:18432
	ds_read_b128 v[108:111], v221 offset:19456
	ds_read_b128 v[112:115], v221 offset:20480
	ds_read_b128 v[116:119], v221 offset:21504
	ds_read_b128 v[120:123], v221 offset:22528
	ds_read_b128 v[124:127], v221 offset:23552
	s_add_i32 m0, s59, 0x10000
	s_nop 0
	global_load_lds_dwordx4 v216, s[52:53]
	s_nop 0
	s_add_i32 m0, s59, 0x12000
	s_nop 0
	global_load_lds_dwordx4 v218, s[52:53]
	s_add_u32 s52, s8, 0x40100
	s_addc_u32 s53, s9, 0
	s_add_i32 m0, s59, 0x14000
	s_nop 0
	global_load_lds_dwordx4 v216, s[52:53]
	s_nop 0
	s_add_i32 m0, s59, 0x16000
	s_nop 0
	global_load_lds_dwordx4 v218, s[52:53]
	s_nop 0
	s_add_i32 m0, s59, 0
	s_nop 0
	global_load_lds_dwordx4 v215, s[46:47]
	s_nop 0
	s_add_i32 m0, s59, 0x2000
	s_nop 0
	global_load_lds_dwordx4 v217, s[46:47]
	s_waitcnt vmcnt(8) lgkmcnt(0)
	s_barrier
	v_mfma_i32_16x16x64_i8 v[136:139], v[0:3], v[104:107], 0
	v_mfma_i32_16x16x64_i8 v[228:231], v[4:7], v[108:111], v[136:139]
	v_mfma_i32_16x16x64_i8 v[136:139], v[8:11], v[104:107], 0
	v_mfma_i32_16x16x64_i8 v[128:131], v[0:3], v[60:63], 0
	v_mfma_i32_16x16x64_i8 v[132:135], v[8:11], v[60:63], 0
	v_mfma_i32_16x16x64_i8 v[232:235], v[12:15], v[108:111], v[136:139]
	v_mfma_i32_16x16x64_i8 v[136:139], v[0:3], v[112:115], 0
	v_mfma_i32_16x16x64_i8 v[0:3], v[0:3], v[120:123], 0
	v_mfma_i32_16x16x64_i8 v[128:131], v[4:7], v[100:103], v[128:131]
	v_mfma_i32_16x16x64_i8 v[132:135], v[12:15], v[100:103], v[132:135]
	v_mfma_i32_16x16x64_i8 v[236:239], v[4:7], v[116:119], v[136:139]
	v_mfma_i32_16x16x64_i8 v[136:139], v[8:11], v[112:115], 0
	v_mfma_i32_16x16x64_i8 v[0:3], v[4:7], v[124:127], v[0:3]
	v_mfma_i32_16x16x64_i8 v[4:7], v[8:11], v[120:123], 0
	v_mfma_i32_16x16x64_i8 v[240:243], v[12:15], v[116:119], v[136:139]
	v_mfma_i32_16x16x64_i8 v[4:7], v[12:15], v[124:127], v[4:7]
	v_mfma_i32_16x16x64_i8 v[8:11], v[16:19], v[60:63], 0
	v_mfma_i32_16x16x64_i8 v[12:15], v[24:27], v[60:63], 0
	v_mfma_i32_16x16x64_i8 v[8:11], v[20:23], v[100:103], v[8:11]
	v_mfma_i32_16x16x64_i8 v[12:15], v[28:31], v[100:103], v[12:15]
	v_mfma_i32_16x16x64_i8 v[60:63], v[16:19], v[104:107], 0
	v_mfma_i32_16x16x64_i8 v[100:103], v[24:27], v[104:107], 0
	v_mfma_i32_16x16x64_i8 v[104:107], v[16:19], v[112:115], 0
	v_mfma_i32_16x16x64_i8 v[16:19], v[16:19], v[120:123], 0
	v_mfma_i32_16x16x64_i8 v[60:63], v[20:23], v[108:111], v[60:63]
	v_mfma_i32_16x16x64_i8 v[100:103], v[28:31], v[108:111], v[100:103]
	v_mfma_i32_16x16x64_i8 v[244:247], v[20:23], v[116:119], v[104:107]
	v_mfma_i32_16x16x64_i8 v[104:107], v[24:27], v[112:115], 0
	v_mfma_i32_16x16x64_i8 v[16:19], v[20:23], v[124:127], v[16:19]
	v_mfma_i32_16x16x64_i8 v[20:23], v[24:27], v[120:123], 0
	v_mfma_i32_16x16x64_i8 v[248:251], v[28:31], v[116:119], v[104:107]
	v_mfma_i32_16x16x64_i8 v[20:23], v[28:31], v[124:127], v[20:23]
	s_barrier
	ds_read_b128 v[24:27], v222
	ds_read_b128 v[28:31], v222 offset:1024
	ds_read_b128 v[112:115], v222 offset:2048
	ds_read_b128 v[116:119], v222 offset:3072
	ds_read_b128 v[208:211], v223
	ds_read_b128 v[224:227], v223 offset:1024
	ds_read_b128 v[64:67], v223 offset:2048
	ds_read_b128 v[68:71], v223 offset:3072
	ds_read_b128 v[104:107], v221 offset:32768
	ds_read_b128 v[108:111], v221 offset:33792
	ds_read_b128 v[120:123], v221 offset:34816
	ds_read_b128 v[124:127], v221 offset:35840
	ds_read_b128 v[136:139], v221 offset:36864
	ds_read_b128 v[148:151], v221 offset:37888
	ds_read_b128 v[72:75], v221 offset:38912
	ds_read_b128 v[76:79], v221 offset:39936
	s_add_u32 s12, s12, 0x40100
	s_addc_u32 s13, s13, 0
	s_add_i32 m0, s59, 0x4000
	s_nop 0
	global_load_lds_dwordx4 v215, s[12:13]
	s_nop 0
	s_add_i32 m0, s59, 0x6000
	s_nop 0
	global_load_lds_dwordx4 v217, s[12:13]
	s_waitcnt vmcnt(8) lgkmcnt(0)
	s_barrier
	v_mfma_i32_16x16x64_i8 v[140:143], v[24:27], v[104:107], v[140:143]
	v_mfma_i32_16x16x64_i8 v[80:83], v[24:27], v[136:139], v[80:83]
	v_mfma_i32_16x16x64_i8 v[204:207], v[28:31], v[108:111], v[140:143]
	v_mfma_i32_16x16x64_i8 v[140:143], v[112:115], v[104:107], v[144:147]
	v_mfma_i32_16x16x64_i8 v[172:175], v[28:31], v[148:151], v[80:83]
	v_mfma_i32_16x16x64_i8 v[80:83], v[112:115], v[136:139], v[84:87]
	v_mfma_i32_16x16x64_i8 v[200:203], v[116:119], v[108:111], v[140:143]
	v_mfma_i32_16x16x64_i8 v[140:143], v[24:27], v[120:123], v[152:155]
	v_mfma_i32_16x16x64_i8 v[168:171], v[116:119], v[148:151], v[80:83]
	v_mfma_i32_16x16x64_i8 v[80:83], v[24:27], v[72:75], v[88:91]
	v_mfma_i32_16x16x64_i8 v[188:191], v[28:31], v[124:127], v[140:143]
	v_mfma_i32_16x16x64_i8 v[140:143], v[112:115], v[120:123], v[156:159]
	v_mfma_i32_16x16x64_i8 v[156:159], v[28:31], v[76:79], v[80:83]
	v_mfma_i32_16x16x64_i8 v[80:83], v[112:115], v[72:75], v[92:95]
	v_mfma_i32_16x16x64_i8 v[184:187], v[116:119], v[124:127], v[140:143]
	v_mfma_i32_16x16x64_i8 v[152:155], v[116:119], v[76:79], v[80:83]
	v_mfma_i32_16x16x64_i8 v[32:35], v[64:67], v[104:107], v[32:35]
	v_mfma_i32_16x16x64_i8 v[192:195], v[68:71], v[108:111], v[32:35]
	v_mfma_i32_16x16x64_i8 v[32:35], v[208:211], v[120:123], v[36:39]
	v_mfma_i32_16x16x64_i8 v[180:183], v[224:227], v[124:127], v[32:35]
	v_mfma_i32_16x16x64_i8 v[32:35], v[64:67], v[120:123], v[40:43]
	v_mfma_i32_16x16x64_i8 v[176:179], v[68:71], v[124:127], v[32:35]
	v_mfma_i32_16x16x64_i8 v[32:35], v[208:211], v[136:139], v[44:47]
	v_mfma_i32_16x16x64_i8 v[164:167], v[224:227], v[148:151], v[32:35]
	v_mfma_i32_16x16x64_i8 v[32:35], v[64:67], v[136:139], v[48:51]
	v_mfma_i32_16x16x64_i8 v[160:163], v[68:71], v[148:151], v[32:35]
	v_mfma_i32_16x16x64_i8 v[32:35], v[208:211], v[72:75], v[52:55]
	v_mfma_i32_16x16x64_i8 v[80:83], v[208:211], v[104:107], v[96:99]
	v_mfma_i32_16x16x64_i8 v[148:151], v[224:227], v[76:79], v[32:35]
	v_mfma_i32_16x16x64_i8 v[32:35], v[64:67], v[72:75], v[56:59]
	v_mfma_i32_16x16x64_i8 v[196:199], v[224:227], v[108:111], v[80:83]
	v_mfma_i32_16x16x64_i8 v[144:147], v[68:71], v[76:79], v[32:35]
	s_barrier
	s_nop 3
	ds_read_b128 v[32:35], v221 offset:49152
	ds_read_b128 v[36:39], v221 offset:50176
	ds_read_b128 v[40:43], v221 offset:51200
	ds_read_b128 v[44:47], v221 offset:52224
	ds_read_b128 v[48:51], v221 offset:53248
	ds_read_b128 v[52:55], v221 offset:54272
	ds_read_b128 v[56:59], v221 offset:55296
	ds_read_b128 v[76:79], v221 offset:56320
	s_add_i32 m0, s59, 0x18000
	s_nop 0
	global_load_lds_dwordx4 v216, s[50:51]
	s_nop 0
	s_add_i32 m0, s59, 0x1a000
	s_nop 0
	global_load_lds_dwordx4 v218, s[50:51]
	s_add_u32 s12, s8, 0x40180
	s_addc_u32 s13, s9, 0
	s_add_i32 m0, s59, 0x1c000
	s_nop 0
	global_load_lds_dwordx4 v216, s[12:13]
	s_nop 0
	s_add_i32 m0, s59, 0x1e000
	s_nop 0
	global_load_lds_dwordx4 v218, s[12:13]
	s_nop 0
	s_add_i32 m0, s59, 0x8000
	s_nop 0
	global_load_lds_dwordx4 v215, s[48:49]
	s_nop 0
	s_add_i32 m0, s59, 0xa000
	s_nop 0
	global_load_lds_dwordx4 v217, s[48:49]
	s_waitcnt vmcnt(8) lgkmcnt(0)
	s_barrier
	v_mfma_i32_16x16x64_i8 v[72:75], v[24:27], v[32:35], v[128:131]
	v_mfma_i32_16x16x64_i8 v[140:143], v[28:31], v[36:39], v[72:75]
	v_mfma_i32_16x16x64_i8 v[72:75], v[112:115], v[32:35], v[132:135]
	v_mfma_i32_16x16x64_i8 v[136:139], v[116:119], v[36:39], v[72:75]
	v_mfma_i32_16x16x64_i8 v[72:75], v[24:27], v[40:43], v[228:231]
	v_mfma_i32_16x16x64_i8 v[124:127], v[28:31], v[44:47], v[72:75]
	v_mfma_i32_16x16x64_i8 v[72:75], v[112:115], v[40:43], v[232:235]
	v_mfma_i32_16x16x64_i8 v[120:123], v[116:119], v[44:47], v[72:75]
	v_mfma_i32_16x16x64_i8 v[72:75], v[24:27], v[48:51], v[236:239]
	v_mfma_i32_16x16x64_i8 v[0:3], v[24:27], v[56:59], v[0:3]
	v_mfma_i32_16x16x64_i8 v[108:111], v[28:31], v[52:55], v[72:75]
	v_mfma_i32_16x16x64_i8 v[72:75], v[112:115], v[48:51], v[240:243]
	v_mfma_i32_16x16x64_i8 v[88:91], v[28:31], v[76:79], v[0:3]
	v_mfma_i32_16x16x64_i8 v[0:3], v[112:115], v[56:59], v[4:7]
	v_mfma_i32_16x16x64_i8 v[104:107], v[116:119], v[52:55], v[72:75]
	v_mfma_i32_16x16x64_i8 v[84:87], v[116:119], v[76:79], v[0:3]
	v_mfma_i32_16x16x64_i8 v[0:3], v[208:211], v[32:35], v[8:11]
	v_mfma_i32_16x16x64_i8 v[132:135], v[224:227], v[36:39], v[0:3]
	v_mfma_i32_16x16x64_i8 v[0:3], v[64:67], v[32:35], v[12:15]
	v_mfma_i32_16x16x64_i8 v[128:131], v[68:71], v[36:39], v[0:3]
	v_mfma_i32_16x16x64_i8 v[0:3], v[208:211], v[40:43], v[60:63]
	v_mfma_i32_16x16x64_i8 v[116:119], v[224:227], v[44:47], v[0:3]
	v_mfma_i32_16x16x64_i8 v[0:3], v[64:67], v[40:43], v[100:103]
	v_mfma_i32_16x16x64_i8 v[112:115], v[68:71], v[44:47], v[0:3]
	v_mfma_i32_16x16x64_i8 v[0:3], v[208:211], v[48:51], v[244:247]
	v_mfma_i32_16x16x64_i8 v[100:103], v[224:227], v[52:55], v[0:3]
	v_mfma_i32_16x16x64_i8 v[0:3], v[64:67], v[48:51], v[248:251]
	v_mfma_i32_16x16x64_i8 v[96:99], v[68:71], v[52:55], v[0:3]
	v_mfma_i32_16x16x64_i8 v[0:3], v[208:211], v[56:59], v[16:19]
	v_mfma_i32_16x16x64_i8 v[72:75], v[224:227], v[76:79], v[0:3]
	v_mfma_i32_16x16x64_i8 v[0:3], v[64:67], v[56:59], v[20:23]
	v_mfma_i32_16x16x64_i8 v[68:71], v[68:71], v[76:79], v[0:3]
	s_barrier
	s_add_u32 s77, s8, 0x200
	s_addc_u32 s80, s9, 0

.LBB0_1108:
	s_ashr_i32 s23, s22, 31
	s_lshl_b64 s[24:25], s[22:23], 20
	s_add_u32 s24, s42, s24
	s_addc_u32 s25, s43, s25
	s_and_b64 s[26:27], s[4:5], exec
	ds_read_b128 v[0:3], v143
	ds_read_b128 v[4:7], v143 offset:1024
	ds_read_b128 v[8:11], v143 offset:2048
	ds_read_b128 v[12:15], v143 offset:3072
	ds_read_b128 v[16:19], v144
	ds_read_b128 v[20:23], v144 offset:1024
	ds_read_b128 v[24:27], v144 offset:2048
	ds_read_b128 v[28:31], v144 offset:3072
	s_cselect_b32 s23, s25, s31
	s_cselect_b32 s51, s24, s30
	s_ashr_i32 s21, s20, 31
	s_lshl_b64 s[26:27], s[20:21], 20
	s_add_u32 s26, s44, s26
	s_addc_u32 s27, s45, s27
	s_and_b64 s[36:37], s[4:5], exec
	s_cselect_b32 s21, s27, s35
	s_cselect_b32 s52, s26, s34
	s_add_u32 s40, s30, 0x100
	s_addc_u32 s41, s31, 0
	s_add_u32 s54, s34, 0x100
	s_addc_u32 s55, s35, 0
	s_add_u32 s36, s30, 0x180
	s_addc_u32 s37, s31, 0
	ds_read_b128 v[32:35], v145
	ds_read_b128 v[36:39], v145 offset:1024
	ds_read_b128 v[40:43], v145 offset:2048
	ds_read_b128 v[44:47], v145 offset:3072
	ds_read_b128 v[48:51], v145 offset:4096
	ds_read_b128 v[52:55], v145 offset:5120
	ds_read_b128 v[56:59], v145 offset:6144
	ds_read_b128 v[60:63], v145 offset:7168
	s_add_u32 s38, s34, 0x180
	s_addc_u32 s39, s35, 0
	s_add_u32 s56, s30, 0x80080
	s_addc_u32 s57, s31, 0
	s_add_i32 m0, s2, 0xc000
	s_nop 0
	global_load_lds_dwordx4 v139, s[56:57]
	s_nop 0
	s_add_i32 m0, s2, 0xe000
	s_nop 0
	global_load_lds_dwordx4 v141, s[56:57]
	s_waitcnt vmcnt(8) lgkmcnt(0)
	s_barrier
	v_mfma_f32_16x16x32_bf16 v[64:67], v[0:3], v[32:35], 0
	v_mfma_f32_16x16x32_bf16 v[68:71], v[8:11], v[32:35], 0
	v_mfma_f32_16x16x32_bf16 v[76:79], v[8:11], v[40:43], 0
	v_mfma_f32_16x16x32_bf16 v[72:75], v[0:3], v[40:43], 0
	v_mfma_f32_16x16x32_bf16 v[80:83], v[0:3], v[48:51], 0
	v_mfma_f32_16x16x32_bf16 v[84:87], v[8:11], v[48:51], 0
	v_mfma_f32_16x16x32_bf16 v[92:95], v[8:11], v[56:59], 0
	v_mfma_f32_16x16x32_bf16 v[88:91], v[0:3], v[56:59], 0
	v_mfma_f32_16x16x32_bf16 v[64:67], v[4:7], v[36:39], v[64:67]
	v_mfma_f32_16x16x32_bf16 v[68:71], v[12:15], v[36:39], v[68:71]
	v_mfma_f32_16x16x32_bf16 v[76:79], v[12:15], v[44:47], v[76:79]
	v_mfma_f32_16x16x32_bf16 v[72:75], v[4:7], v[44:47], v[72:75]
	v_mfma_f32_16x16x32_bf16 v[80:83], v[4:7], v[52:55], v[80:83]
	v_mfma_f32_16x16x32_bf16 v[84:87], v[12:15], v[52:55], v[84:87]
	v_mfma_f32_16x16x32_bf16 v[96:99], v[12:15], v[60:63], v[92:95]
	v_mfma_f32_16x16x32_bf16 v[88:91], v[4:7], v[60:63], v[88:91]
	v_mfma_f32_16x16x32_bf16 v[92:95], v[16:19], v[32:35], 0
	v_mfma_f32_16x16x32_bf16 v[32:35], v[24:27], v[32:35], 0
	v_mfma_f32_16x16x32_bf16 v[104:107], v[20:23], v[36:39], v[92:95]
	v_mfma_f32_16x16x32_bf16 v[32:35], v[28:31], v[36:39], v[32:35]
	v_mfma_f32_16x16x32_bf16 v[36:39], v[16:19], v[40:43], 0
	v_mfma_f32_16x16x32_bf16 v[40:43], v[24:27], v[40:43], 0
	v_mfma_f32_16x16x32_bf16 v[36:39], v[20:23], v[44:47], v[36:39]
	v_mfma_f32_16x16x32_bf16 v[40:43], v[28:31], v[44:47], v[40:43]
	v_mfma_f32_16x16x32_bf16 v[44:47], v[16:19], v[48:51], 0
	v_mfma_f32_16x16x32_bf16 v[48:51], v[24:27], v[48:51], 0
	v_mfma_f32_16x16x32_bf16 v[44:47], v[20:23], v[52:55], v[44:47]
	v_mfma_f32_16x16x32_bf16 v[48:51], v[28:31], v[52:55], v[48:51]
	v_mfma_f32_16x16x32_bf16 v[52:55], v[16:19], v[56:59], 0
	v_mfma_f32_16x16x32_bf16 v[56:59], v[24:27], v[56:59], 0
	v_mfma_f32_16x16x32_bf16 v[52:55], v[20:23], v[60:63], v[52:55]
	v_mfma_f32_16x16x32_bf16 v[60:63], v[28:31], v[60:63], v[56:59]
	s_barrier
	s_nop 3
	ds_read_b128 v[56:59], v145 offset:16384
	ds_read_b128 v[92:95], v145 offset:17408
	ds_read_b128 v[100:103], v145 offset:18432
	ds_read_b128 v[108:111], v145 offset:19456
	ds_read_b128 v[112:115], v145 offset:20480
	ds_read_b128 v[116:119], v145 offset:21504
	ds_read_b128 v[120:123], v145 offset:22528
	ds_read_b128 v[124:127], v145 offset:23552
	s_add_i32 m0, s2, 0x10000
	s_nop 0
	global_load_lds_dwordx4 v140, s[54:55]
	s_nop 0
	s_add_i32 m0, s2, 0x12000
	s_nop 0
	global_load_lds_dwordx4 v142, s[54:55]
	s_add_u32 s54, s34, 0x80100
	s_addc_u32 s55, s35, 0
	s_add_i32 m0, s2, 0x14000
	s_nop 0
	global_load_lds_dwordx4 v140, s[54:55]
	s_nop 0
	s_add_i32 m0, s2, 0x16000
	s_nop 0
	global_load_lds_dwordx4 v142, s[54:55]
	s_nop 0
	s_add_i32 m0, s2, 0
	s_nop 0
	global_load_lds_dwordx4 v139, s[40:41]
	s_nop 0
	s_add_i32 m0, s2, 0x2000
	s_nop 0
	global_load_lds_dwordx4 v141, s[40:41]
	s_waitcnt vmcnt(8) lgkmcnt(0)
	s_barrier
	v_mfma_f32_16x16x32_bf16 v[132:135], v[0:3], v[56:59], 0
	v_mfma_f32_16x16x32_bf16 v[152:155], v[0:3], v[100:103], 0
	v_mfma_f32_16x16x32_bf16 v[160:163], v[0:3], v[112:115], 0
	v_mfma_f32_16x16x32_bf16 v[0:3], v[0:3], v[120:123], 0
	v_mfma_f32_16x16x32_bf16 v[132:135], v[4:7], v[92:95], v[132:135]
	v_mfma_f32_16x16x32_bf16 v[152:155], v[4:7], v[108:111], v[152:155]
	v_mfma_f32_16x16x32_bf16 v[160:163], v[4:7], v[116:119], v[160:163]
	v_mfma_f32_16x16x32_bf16 v[0:3], v[4:7], v[124:127], v[0:3]
	v_mfma_f32_16x16x32_bf16 v[4:7], v[8:11], v[120:123], 0
	v_mfma_f32_16x16x32_bf16 v[148:151], v[8:11], v[56:59], 0
	v_mfma_f32_16x16x32_bf16 v[156:159], v[8:11], v[100:103], 0
	v_mfma_f32_16x16x32_bf16 v[164:167], v[8:11], v[112:115], 0
	v_mfma_f32_16x16x32_bf16 v[4:7], v[12:15], v[124:127], v[4:7]
	v_mfma_f32_16x16x32_bf16 v[148:151], v[12:15], v[92:95], v[148:151]
	v_mfma_f32_16x16x32_bf16 v[156:159], v[12:15], v[108:111], v[156:159]
	v_mfma_f32_16x16x32_bf16 v[164:167], v[12:15], v[116:119], v[164:167]
	v_mfma_f32_16x16x32_bf16 v[12:15], v[24:27], v[56:59], 0
	v_mfma_f32_16x16x32_bf16 v[168:171], v[28:31], v[92:95], v[12:15]
	v_mfma_f32_16x16x32_bf16 v[12:15], v[16:19], v[100:103], 0
	v_mfma_f32_16x16x32_bf16 v[172:175], v[20:23], v[108:111], v[12:15]
	v_mfma_f32_16x16x32_bf16 v[12:15], v[24:27], v[100:103], 0
	v_mfma_f32_16x16x32_bf16 v[176:179], v[28:31], v[108:111], v[12:15]
	v_mfma_f32_16x16x32_bf16 v[12:15], v[16:19], v[112:115], 0
	v_mfma_f32_16x16x32_bf16 v[180:183], v[20:23], v[116:119], v[12:15]
	v_mfma_f32_16x16x32_bf16 v[12:15], v[24:27], v[112:115], 0
	v_mfma_f32_16x16x32_bf16 v[8:11], v[16:19], v[56:59], 0
	v_mfma_f32_16x16x32_bf16 v[184:187], v[28:31], v[116:119], v[12:15]
	v_mfma_f32_16x16x32_bf16 v[12:15], v[16:19], v[120:123], 0
	v_mfma_f32_16x16x32_bf16 v[8:11], v[20:23], v[92:95], v[8:11]
	v_mfma_f32_16x16x32_bf16 v[188:191], v[20:23], v[124:127], v[12:15]
	v_mfma_f32_16x16x32_bf16 v[12:15], v[24:27], v[120:123], 0
	v_mfma_f32_16x16x32_bf16 v[192:195], v[28:31], v[124:127], v[12:15]
	s_barrier
	s_nop 4
	ds_read_b128 v[12:15], v146
	ds_read_b128 v[16:19], v146 offset:1024
	ds_read_b128 v[24:27], v146 offset:2048
	ds_read_b128 v[196:199], v146 offset:3072
	ds_read_b128 v[200:203], v147
	ds_read_b128 v[204:207], v147 offset:1024
	ds_read_b128 v[208:211], v147 offset:2048
	ds_read_b128 v[212:215], v147 offset:3072
	ds_read_b128 v[20:23], v145 offset:32768
	ds_read_b128 v[28:31], v145 offset:33792
	ds_read_b128 v[216:219], v145 offset:34816
	ds_read_b128 v[220:223], v145 offset:35840
	ds_read_b128 v[224:227], v145 offset:36864
	ds_read_b128 v[228:231], v145 offset:37888
	ds_read_b128 v[232:235], v145 offset:38912
	ds_read_b128 v[236:239], v145 offset:39936
	s_add_u32 s40, s30, 0x80100
	s_addc_u32 s41, s31, 0
	s_add_i32 m0, s2, 0x4000
	s_nop 0
	global_load_lds_dwordx4 v139, s[40:41]
	s_nop 0
	s_add_i32 m0, s2, 0x6000
	s_nop 0
	global_load_lds_dwordx4 v141, s[40:41]
	s_waitcnt vmcnt(8) lgkmcnt(0)
	s_barrier
	v_mfma_f32_16x16x32_bf16 v[56:59], v[12:15], v[20:23], v[64:67]
	v_mfma_f32_16x16x32_bf16 v[116:119], v[16:19], v[28:31], v[56:59]
	v_mfma_f32_16x16x32_bf16 v[56:59], v[24:27], v[20:23], v[68:71]
	v_mfma_f32_16x16x32_bf16 v[112:115], v[196:199], v[28:31], v[56:59]
	v_mfma_f32_16x16x32_bf16 v[56:59], v[12:15], v[216:219], v[72:75]
	v_mfma_f32_16x16x32_bf16 v[108:111], v[16:19], v[220:223], v[56:59]
	v_mfma_f32_16x16x32_bf16 v[56:59], v[24:27], v[216:219], v[76:79]
	v_mfma_f32_16x16x32_bf16 v[100:103], v[196:199], v[220:223], v[56:59]
	v_mfma_f32_16x16x32_bf16 v[56:59], v[12:15], v[224:227], v[80:83]
	v_mfma_f32_16x16x32_bf16 v[92:95], v[16:19], v[228:231], v[56:59]
	v_mfma_f32_16x16x32_bf16 v[56:59], v[24:27], v[224:227], v[84:87]
	v_mfma_f32_16x16x32_bf16 v[84:87], v[196:199], v[228:231], v[56:59]
	v_mfma_f32_16x16x32_bf16 v[56:59], v[12:15], v[232:235], v[88:91]
	v_mfma_f32_16x16x32_bf16 v[72:75], v[16:19], v[236:239], v[56:59]
	v_mfma_f32_16x16x32_bf16 v[56:59], v[24:27], v[232:235], v[96:99]
	v_mfma_f32_16x16x32_bf16 v[56:59], v[196:199], v[236:239], v[56:59]
	v_mfma_f32_16x16x32_bf16 v[64:67], v[200:203], v[20:23], v[104:107]
	v_mfma_f32_16x16x32_bf16 v[20:23], v[208:211], v[20:23], v[32:35]
	v_mfma_f32_16x16x32_bf16 v[120:123], v[212:215], v[28:31], v[20:23]
	v_mfma_f32_16x16x32_bf16 v[20:23], v[200:203], v[216:219], v[36:39]
	v_mfma_f32_16x16x32_bf16 v[104:107], v[204:207], v[220:223], v[20:23]
	v_mfma_f32_16x16x32_bf16 v[20:23], v[208:211], v[216:219], v[40:43]
	v_mfma_f32_16x16x32_bf16 v[96:99], v[212:215], v[220:223], v[20:23]
	v_mfma_f32_16x16x32_bf16 v[20:23], v[200:203], v[224:227], v[44:47]
	v_mfma_f32_16x16x32_bf16 v[88:91], v[204:207], v[228:231], v[20:23]
	v_mfma_f32_16x16x32_bf16 v[20:23], v[208:211], v[224:227], v[48:51]
	v_mfma_f32_16x16x32_bf16 v[80:83], v[212:215], v[228:231], v[20:23]
	v_mfma_f32_16x16x32_bf16 v[20:23], v[200:203], v[232:235], v[52:55]
	v_mfma_f32_16x16x32_bf16 v[124:127], v[204:207], v[28:31], v[64:67]
	v_mfma_f32_16x16x32_bf16 v[64:67], v[204:207], v[236:239], v[20:23]
	v_mfma_f32_16x16x32_bf16 v[20:23], v[208:211], v[232:235], v[60:63]
	v_mfma_f32_16x16x32_bf16 v[48:51], v[212:215], v[236:239], v[20:23]
	s_barrier
	ds_read_b128 v[32:35], v145 offset:49152
	ds_read_b128 v[40:43], v145 offset:50176
	ds_read_b128 v[216:219], v145 offset:51200
	ds_read_b128 v[220:223], v145 offset:52224
	ds_read_b128 v[224:227], v145 offset:53248
	ds_read_b128 v[228:231], v145 offset:54272
	ds_read_b128 v[232:235], v145 offset:55296
	ds_read_b128 v[236:239], v145 offset:56320
	s_add_i32 m0, s2, 0x18000
	s_nop 0
	global_load_lds_dwordx4 v140, s[38:39]
	s_nop 0
	s_add_i32 m0, s2, 0x1a000
	s_nop 0
	global_load_lds_dwordx4 v142, s[38:39]
	s_add_u32 s38, s34, 0x80180
	s_addc_u32 s39, s35, 0
	s_add_i32 m0, s2, 0x1c000
	s_nop 0
	global_load_lds_dwordx4 v140, s[38:39]
	s_nop 0
	s_add_i32 m0, s2, 0x1e000
	s_nop 0
	global_load_lds_dwordx4 v142, s[38:39]
	s_nop 0
	s_add_i32 m0, s2, 0x8000
	s_nop 0
	global_load_lds_dwordx4 v139, s[36:37]
	s_nop 0
	s_add_i32 m0, s2, 0xa000
	s_nop 0
	global_load_lds_dwordx4 v141, s[36:37]
	s_waitcnt vmcnt(8) lgkmcnt(0)
	s_barrier
	v_mfma_f32_16x16x32_bf16 v[20:23], v[12:15], v[32:35], v[132:135]
	v_mfma_f32_16x16x32_bf16 v[76:79], v[16:19], v[40:43], v[20:23]
	v_mfma_f32_16x16x32_bf16 v[20:23], v[24:27], v[32:35], v[148:151]
	v_mfma_f32_16x16x32_bf16 v[60:63], v[196:199], v[40:43], v[20:23]
	v_mfma_f32_16x16x32_bf16 v[20:23], v[12:15], v[216:219], v[152:155]
	v_mfma_f32_16x16x32_bf16 v[44:47], v[16:19], v[220:223], v[20:23]
	v_mfma_f32_16x16x32_bf16 v[20:23], v[24:27], v[216:219], v[156:159]
	v_mfma_f32_16x16x32_bf16 v[36:39], v[196:199], v[220:223], v[20:23]
	v_mfma_f32_16x16x32_bf16 v[20:23], v[12:15], v[224:227], v[160:163]
	v_mfma_f32_16x16x32_bf16 v[0:3], v[12:15], v[232:235], v[0:3]
	v_mfma_f32_16x16x32_bf16 v[28:31], v[16:19], v[228:231], v[20:23]
	v_mfma_f32_16x16x32_bf16 v[20:23], v[24:27], v[224:227], v[164:167]
	v_mfma_f32_16x16x32_bf16 v[12:15], v[16:19], v[236:239], v[0:3]
	v_mfma_f32_16x16x32_bf16 v[0:3], v[24:27], v[232:235], v[4:7]
	v_mfma_f32_16x16x32_bf16 v[20:23], v[196:199], v[228:231], v[20:23]
	v_mfma_f32_16x16x32_bf16 v[4:7], v[196:199], v[236:239], v[0:3]
	v_mfma_f32_16x16x32_bf16 v[0:3], v[200:203], v[32:35], v[8:11]
	v_mfma_f32_16x16x32_bf16 v[68:71], v[204:207], v[40:43], v[0:3]
	v_mfma_f32_16x16x32_bf16 v[0:3], v[208:211], v[32:35], v[168:171]
	v_mfma_f32_16x16x32_bf16 v[52:55], v[212:215], v[40:43], v[0:3]
	v_mfma_f32_16x16x32_bf16 v[0:3], v[200:203], v[216:219], v[172:175]
	v_mfma_f32_16x16x32_bf16 v[40:43], v[204:207], v[220:223], v[0:3]
	v_mfma_f32_16x16x32_bf16 v[0:3], v[208:211], v[216:219], v[176:179]
	v_mfma_f32_16x16x32_bf16 v[32:35], v[212:215], v[220:223], v[0:3]
	v_mfma_f32_16x16x32_bf16 v[0:3], v[200:203], v[224:227], v[180:183]
	v_mfma_f32_16x16x32_bf16 v[24:27], v[204:207], v[228:231], v[0:3]
	v_mfma_f32_16x16x32_bf16 v[0:3], v[208:211], v[224:227], v[184:187]
	v_mfma_f32_16x16x32_bf16 v[16:19], v[212:215], v[228:231], v[0:3]
	v_mfma_f32_16x16x32_bf16 v[0:3], v[200:203], v[232:235], v[188:191]
	v_mfma_f32_16x16x32_bf16 v[8:11], v[204:207], v[236:239], v[0:3]
	v_mfma_f32_16x16x32_bf16 v[0:3], v[208:211], v[232:235], v[192:195]
	v_mfma_f32_16x16x32_bf16 v[0:3], v[212:215], v[236:239], v[0:3]
	s_barrier
	s_add_u32 s53, s30, 0x200
	s_addc_u32 s54, s31, 0
	s_add_u32 s55, s34, 0x200
	s_addc_u32 s56, s35, 0
	s_add_u32 s30, s30, 0x80180
	s_addc_u32 s31, s31, 0
	s_mov_b32 s57, 0
